# router prologue: first three half-trips' operand loads issued before the accumulator clearing
# speedup vs baseline: 1.0010x; 1.0010x over previous
.LBB0_711:
	v_lshl_add_u64 v[52:53], v[50:51], 0, s[12:13]
	v_add_co_u32_e32 v152, vcc, s42, v52
	v_lshl_add_u64 v[54:55], v[48:49], 0, s[12:13]
	s_nop 0
	v_addc_co_u32_e32 v153, vcc, 0, v53, vcc
	v_add_co_u32_e32 v154, vcc, s45, v52
	s_nop 0
	s_nop 0
	v_addc_co_u32_e32 v155, vcc, 0, v53, vcc
	v_add_co_u32_e32 v156, vcc, s46, v54
	s_nop 0
	s_nop 0
	v_addc_co_u32_e32 v157, vcc, 0, v55, vcc
	v_add_co_u32_e32 v158, vcc, s47, v54
	s_nop 0
	s_nop 0
	v_addc_co_u32_e32 v159, vcc, 0, v55, vcc
	global_load_dwordx4 v[176:179], v[152:153], off
	global_load_dwordx4 v[180:183], v[156:157], off
	global_load_dwordx4 v[184:187], v[154:155], off
	global_load_dwordx4 v[188:191], v[158:159], off
	global_load_dwordx4 v[192:195], v[152:153], off offset:32
	global_load_dwordx4 v[196:199], v[156:157], off offset:32
	global_load_dwordx4 v[200:203], v[154:155], off offset:32
	global_load_dwordx4 v[204:207], v[158:159], off offset:32
	global_load_dwordx4 v[208:211], v[152:153], off offset:64
	global_load_dwordx4 v[212:215], v[156:157], off offset:64
	global_load_dwordx4 v[216:219], v[154:155], off offset:64
	global_load_dwordx4 v[220:223], v[158:159], off offset:64
	global_load_dwordx4 v[224:227], v[152:153], off offset:96
	global_load_dwordx4 v[228:231], v[156:157], off offset:96
	global_load_dwordx4 v[232:235], v[154:155], off offset:96
	global_load_dwordx4 v[236:239], v[158:159], off offset:96
	global_load_dwordx4 v[240:243], v[152:153], off offset:128
	global_load_dwordx4 v[244:247], v[156:157], off offset:128
	global_load_dwordx4 v[248:251], v[154:155], off offset:128
	global_load_dwordx4 v[52:55], v[158:159], off offset:128
	global_load_dwordx4 v[56:59], v[152:153], off offset:160
	global_load_dwordx4 v[60:63], v[156:157], off offset:160
	global_load_dwordx4 v[64:67], v[154:155], off offset:160
	global_load_dwordx4 v[68:71], v[158:159], off offset:160
	v_mov_b32_e32 v3, v2
	v_mov_b32_e32 v4, v2
	v_mov_b32_e32 v5, v2
	v_mov_b32_e32 v6, v2
	v_mov_b32_e32 v7, v2
	v_mov_b32_e32 v8, v2
	v_mov_b32_e32 v9, v2
	v_mov_b32_e32 v10, v2
	v_mov_b32_e32 v11, v2
	v_mov_b32_e32 v12, v2
	v_mov_b32_e32 v13, v2
	v_mov_b32_e32 v14, v2
	v_mov_b32_e32 v15, v2
	v_mov_b32_e32 v16, v2
	v_mov_b32_e32 v17, v2
	v_mov_b32_e32 v18, v2
	v_mov_b32_e32 v19, v2
	v_mov_b32_e32 v20, v2
	v_mov_b32_e32 v21, v2
	v_mov_b32_e32 v22, v2
	v_mov_b32_e32 v23, v2
	v_mov_b32_e32 v24, v2
	v_mov_b32_e32 v25, v2
	v_mov_b32_e32 v26, v2
	v_mov_b32_e32 v27, v2
	v_mov_b32_e32 v28, v2
	v_mov_b32_e32 v29, v2
	v_mov_b32_e32 v30, v2
	v_mov_b32_e32 v31, v2
	v_mov_b32_e32 v32, v2
	v_mov_b32_e32 v33, v2
	s_nop 1
	s_waitcnt vmcnt(16)
	v_mfma_f32_32x32x16_bf16 v[2:17], v[176:179], v[180:183], v[2:17]
	v_mfma_f32_32x32x16_bf16 v[18:33], v[184:187], v[180:183], v[18:33]
	v_mfma_f32_32x32x16_bf16 v[2:17], v[176:179], v[188:191], v[2:17]
	v_mfma_f32_32x32x16_bf16 v[18:33], v[184:187], v[188:191], v[18:33]
	v_mfma_f32_32x32x16_bf16 v[2:17], v[192:195], v[196:199], v[2:17]
	v_mfma_f32_32x32x16_bf16 v[18:33], v[200:203], v[196:199], v[18:33]
	v_mfma_f32_32x32x16_bf16 v[2:17], v[192:195], v[204:207], v[2:17]
	v_mfma_f32_32x32x16_bf16 v[18:33], v[200:203], v[204:207], v[18:33]
	global_load_dwordx4 v[176:179], v[152:153], off offset:192
	global_load_dwordx4 v[180:183], v[156:157], off offset:192
	global_load_dwordx4 v[184:187], v[154:155], off offset:192
	global_load_dwordx4 v[188:191], v[158:159], off offset:192
	global_load_dwordx4 v[192:195], v[152:153], off offset:224
	global_load_dwordx4 v[196:199], v[156:157], off offset:224
	global_load_dwordx4 v[200:203], v[154:155], off offset:224
	global_load_dwordx4 v[204:207], v[158:159], off offset:224
	s_waitcnt vmcnt(16)
	v_mfma_f32_32x32x16_bf16 v[2:17], v[208:211], v[212:215], v[2:17]
	v_mfma_f32_32x32x16_bf16 v[18:33], v[216:219], v[212:215], v[18:33]
	v_mfma_f32_32x32x16_bf16 v[2:17], v[208:211], v[220:223], v[2:17]
	v_mfma_f32_32x32x16_bf16 v[18:33], v[216:219], v[220:223], v[18:33]
	v_mfma_f32_32x32x16_bf16 v[2:17], v[224:227], v[228:231], v[2:17]
	v_mfma_f32_32x32x16_bf16 v[18:33], v[232:235], v[228:231], v[18:33]
	v_mfma_f32_32x32x16_bf16 v[2:17], v[224:227], v[236:239], v[2:17]
	v_mfma_f32_32x32x16_bf16 v[18:33], v[232:235], v[236:239], v[18:33]
	global_load_dwordx4 v[208:211], v[152:153], off offset:256
	global_load_dwordx4 v[212:215], v[156:157], off offset:256
	global_load_dwordx4 v[216:219], v[154:155], off offset:256
	global_load_dwordx4 v[220:223], v[158:159], off offset:256
	global_load_dwordx4 v[224:227], v[152:153], off offset:288
	global_load_dwordx4 v[228:231], v[156:157], off offset:288
	global_load_dwordx4 v[232:235], v[154:155], off offset:288
	global_load_dwordx4 v[236:239], v[158:159], off offset:288
	s_waitcnt vmcnt(16)
	v_mfma_f32_32x32x16_bf16 v[2:17], v[240:243], v[244:247], v[2:17]
	v_mfma_f32_32x32x16_bf16 v[18:33], v[248:251], v[244:247], v[18:33]
	v_mfma_f32_32x32x16_bf16 v[2:17], v[240:243], v[52:55], v[2:17]
	v_mfma_f32_32x32x16_bf16 v[18:33], v[248:251], v[52:55], v[18:33]
	v_mfma_f32_32x32x16_bf16 v[2:17], v[56:59], v[60:63], v[2:17]
	v_mfma_f32_32x32x16_bf16 v[18:33], v[64:67], v[60:63], v[18:33]
	v_mfma_f32_32x32x16_bf16 v[2:17], v[56:59], v[68:71], v[2:17]
	v_mfma_f32_32x32x16_bf16 v[18:33], v[64:67], v[68:71], v[18:33]
	global_load_dwordx4 v[240:243], v[152:153], off offset:320
	global_load_dwordx4 v[244:247], v[156:157], off offset:320
	global_load_dwordx4 v[248:251], v[154:155], off offset:320
	global_load_dwordx4 v[52:55], v[158:159], off offset:320
	global_load_dwordx4 v[56:59], v[152:153], off offset:352
	global_load_dwordx4 v[60:63], v[156:157], off offset:352
	global_load_dwordx4 v[64:67], v[154:155], off offset:352
	global_load_dwordx4 v[68:71], v[158:159], off offset:352
	s_waitcnt vmcnt(16)
	v_mfma_f32_32x32x16_bf16 v[2:17], v[176:179], v[180:183], v[2:17]
	v_mfma_f32_32x32x16_bf16 v[18:33], v[184:187], v[180:183], v[18:33]
	v_mfma_f32_32x32x16_bf16 v[2:17], v[176:179], v[188:191], v[2:17]
	v_mfma_f32_32x32x16_bf16 v[18:33], v[184:187], v[188:191], v[18:33]
	v_mfma_f32_32x32x16_bf16 v[2:17], v[192:195], v[196:199], v[2:17]
	v_mfma_f32_32x32x16_bf16 v[18:33], v[200:203], v[196:199], v[18:33]
	v_mfma_f32_32x32x16_bf16 v[2:17], v[192:195], v[204:207], v[2:17]
	v_mfma_f32_32x32x16_bf16 v[18:33], v[200:203], v[204:207], v[18:33]
	global_load_dwordx4 v[176:179], v[152:153], off offset:384
	global_load_dwordx4 v[180:183], v[156:157], off offset:384
	global_load_dwordx4 v[184:187], v[154:155], off offset:384
	global_load_dwordx4 v[188:191], v[158:159], off offset:384
	global_load_dwordx4 v[192:195], v[152:153], off offset:416
	global_load_dwordx4 v[196:199], v[156:157], off offset:416
	global_load_dwordx4 v[200:203], v[154:155], off offset:416
	global_load_dwordx4 v[204:207], v[158:159], off offset:416
	s_waitcnt vmcnt(16)
	v_mfma_f32_32x32x16_bf16 v[2:17], v[208:211], v[212:215], v[2:17]
	v_mfma_f32_32x32x16_bf16 v[18:33], v[216:219], v[212:215], v[18:33]
	v_mfma_f32_32x32x16_bf16 v[2:17], v[208:211], v[220:223], v[2:17]
	v_mfma_f32_32x32x16_bf16 v[18:33], v[216:219], v[220:223], v[18:33]
	v_mfma_f32_32x32x16_bf16 v[2:17], v[224:227], v[228:231], v[2:17]
	v_mfma_f32_32x32x16_bf16 v[18:33], v[232:235], v[228:231], v[18:33]
	v_mfma_f32_32x32x16_bf16 v[2:17], v[224:227], v[236:239], v[2:17]
	v_mfma_f32_32x32x16_bf16 v[18:33], v[232:235], v[236:239], v[18:33]
	global_load_dwordx4 v[208:211], v[152:153], off offset:448
	global_load_dwordx4 v[212:215], v[156:157], off offset:448
	global_load_dwordx4 v[216:219], v[154:155], off offset:448
	global_load_dwordx4 v[220:223], v[158:159], off offset:448
	global_load_dwordx4 v[224:227], v[152:153], off offset:480
	global_load_dwordx4 v[228:231], v[156:157], off offset:480
	global_load_dwordx4 v[232:235], v[154:155], off offset:480
	global_load_dwordx4 v[236:239], v[158:159], off offset:480
	s_waitcnt vmcnt(16)
	v_mfma_f32_32x32x16_bf16 v[2:17], v[240:243], v[244:247], v[2:17]
	v_mfma_f32_32x32x16_bf16 v[18:33], v[248:251], v[244:247], v[18:33]
	v_mfma_f32_32x32x16_bf16 v[2:17], v[240:243], v[52:55], v[2:17]
	v_mfma_f32_32x32x16_bf16 v[18:33], v[248:251], v[52:55], v[18:33]
	v_mfma_f32_32x32x16_bf16 v[2:17], v[56:59], v[60:63], v[2:17]
	v_mfma_f32_32x32x16_bf16 v[18:33], v[64:67], v[60:63], v[18:33]
	v_mfma_f32_32x32x16_bf16 v[2:17], v[56:59], v[68:71], v[2:17]
	v_mfma_f32_32x32x16_bf16 v[18:33], v[64:67], v[68:71], v[18:33]
	s_waitcnt vmcnt(8)
	v_mfma_f32_32x32x16_bf16 v[2:17], v[176:179], v[180:183], v[2:17]
	v_mfma_f32_32x32x16_bf16 v[18:33], v[184:187], v[180:183], v[18:33]
	v_mfma_f32_32x32x16_bf16 v[2:17], v[176:179], v[188:191], v[2:17]
	v_mfma_f32_32x32x16_bf16 v[18:33], v[184:187], v[188:191], v[18:33]
	v_mfma_f32_32x32x16_bf16 v[2:17], v[192:195], v[196:199], v[2:17]
	v_mfma_f32_32x32x16_bf16 v[18:33], v[200:203], v[196:199], v[18:33]
	v_mfma_f32_32x32x16_bf16 v[2:17], v[192:195], v[204:207], v[2:17]
	v_mfma_f32_32x32x16_bf16 v[18:33], v[200:203], v[204:207], v[18:33]
	s_waitcnt vmcnt(0)
	v_mfma_f32_32x32x16_bf16 v[2:17], v[208:211], v[212:215], v[2:17]
	v_mfma_f32_32x32x16_bf16 v[18:33], v[216:219], v[212:215], v[18:33]
	v_mfma_f32_32x32x16_bf16 v[2:17], v[208:211], v[220:223], v[2:17]
	v_mfma_f32_32x32x16_bf16 v[18:33], v[216:219], v[220:223], v[18:33]
	v_mfma_f32_32x32x16_bf16 v[2:17], v[224:227], v[228:231], v[2:17]
	v_mfma_f32_32x32x16_bf16 v[18:33], v[232:235], v[228:231], v[18:33]
	v_mfma_f32_32x32x16_bf16 v[2:17], v[224:227], v[236:239], v[2:17]
	v_mfma_f32_32x32x16_bf16 v[18:33], v[232:235], v[236:239], v[18:33]
	s_movk_i32 s12, 0x200
	s_mov_b32 s13, 0
	s_cmpk_eq_i32 s12, 0x200
	s_nop 9
	ds_write2_b32 v74, v2, v3 offset1:32
	v_add_u32_e32 v2, 0x1000, v74
	ds_write2_b32 v2, v18, v19 offset1:32
	ds_write2_b32 v74, v4, v5 offset0:64 offset1:96
	ds_write2_b32 v2, v20, v21 offset0:64 offset1:96
	v_add_u32_e32 v2, 0x400, v74
	v_add_u32_e32 v3, 0x1400, v74
	ds_write2_b32 v2, v6, v7 offset1:32
	ds_write2_b32 v3, v22, v23 offset1:32
	ds_write2_b32 v2, v8, v9 offset0:64 offset1:96
	ds_write2_b32 v3, v24, v25 offset0:64 offset1:96
	v_add_u32_e32 v2, 0x800, v74
	v_add_u32_e32 v3, 0x1800, v74
	ds_write2_b32 v2, v10, v11 offset1:32
	ds_write2_b32 v3, v26, v27 offset1:32
	ds_write2_b32 v2, v12, v13 offset0:64 offset1:96
	ds_write2_b32 v3, v28, v29 offset0:64 offset1:96
	v_add_u32_e32 v2, 0xc00, v74
	v_add_u32_e32 v3, 0x1c00, v74
	ds_write2_b32 v2, v14, v15 offset1:32
	ds_write2_b32 v3, v30, v31 offset1:32
	ds_write2_b32 v2, v16, v17 offset0:64 offset1:96
	ds_write2_b32 v3, v32, v33 offset0:64 offset1:96
	s_waitcnt lgkmcnt(0)
	s_barrier
	ds_read2st64_b32 v[2:3], v76 offset1:32
	ds_read2st64_b32 v[4:5], v76 offset0:64 offset1:96
	ds_read2st64_b32 v[6:7], v76 offset0:128 offset1:160
	s_waitcnt lgkmcnt(2)
	v_add_f32_e32 v2, 0, v2
	v_add_f32_e32 v8, v2, v3
	ds_read2st64_b32 v[2:3], v76 offset0:192 offset1:224
	s_waitcnt lgkmcnt(2)
	v_add_f32_e32 v4, v8, v4
	v_add_f32_e32 v4, v4, v5
	s_waitcnt lgkmcnt(1)
	v_add_f32_e32 v4, v4, v6
	v_add_f32_e32 v4, v4, v7
	s_waitcnt lgkmcnt(0)
	v_add_f32_e32 v2, v4, v2
	v_add_f32_e32 v14, v2, v3
	ds_read_b64 v[2:3], v138
	ds_read2_b32 v[4:5], v75 offset1:32
	ds_read2st64_b32 v[6:7], v78 offset1:32
	ds_read_b64 v[8:9], v139
	ds_read_b64 v[10:11], v140
	ds_read_b64 v[12:13], v141
	s_waitcnt lgkmcnt(4)
	v_fma_f32 v2, -v2, v4, v14
	v_fma_f32 v2, v3, v2, v5
	ds_write_b32 v77, v2
	ds_read2st64_b32 v[2:3], v78 offset0:64 offset1:96
	ds_read2st64_b32 v[14:15], v78 offset0:128 offset1:160
	s_waitcnt lgkmcnt(6)
	v_add_f32_e32 v6, 0, v6
	v_add_f32_e32 v16, v6, v7
	ds_read2st64_b32 v[6:7], v78 offset0:192 offset1:224
	s_waitcnt lgkmcnt(2)
	v_add_f32_e32 v2, v16, v2
	v_add_f32_e32 v2, v2, v3
	s_waitcnt lgkmcnt(1)
	v_add_f32_e32 v2, v2, v14
	v_add_f32_e32 v2, v2, v15
	s_waitcnt lgkmcnt(0)
	v_add_f32_e32 v2, v2, v6
	v_add_f32_e32 v6, v2, v7
	ds_read2st64_b32 v[2:3], v80 offset1:32
	v_fma_f32 v6, -v4, v8, v6
	v_fma_f32 v6, v9, v6, v5
	ds_write_b32 v79, v6
	ds_read2st64_b32 v[6:7], v80 offset0:64 offset1:96
	ds_read2st64_b32 v[8:9], v80 offset0:128 offset1:160
	s_waitcnt lgkmcnt(3)
	v_add_f32_e32 v2, 0, v2
	v_add_f32_e32 v14, v2, v3
	ds_read2st64_b32 v[2:3], v80 offset0:192 offset1:224
	s_waitcnt lgkmcnt(2)
	v_add_f32_e32 v6, v14, v6
	v_add_f32_e32 v6, v6, v7
	s_waitcnt lgkmcnt(1)
	v_add_f32_e32 v6, v6, v8
	v_add_f32_e32 v6, v6, v9
	s_waitcnt lgkmcnt(0)
	v_add_f32_e32 v2, v6, v2
	v_add_f32_e32 v6, v2, v3
	ds_read2st64_b32 v[2:3], v82 offset1:32
	v_fma_f32 v6, -v4, v10, v6
	v_fma_f32 v6, v11, v6, v5
	ds_write_b32 v81, v6
	ds_read2st64_b32 v[6:7], v82 offset0:64 offset1:96
	ds_read2st64_b32 v[8:9], v82 offset0:128 offset1:160
	s_waitcnt lgkmcnt(3)
	v_add_f32_e32 v2, 0, v2
	v_add_f32_e32 v10, v2, v3
	ds_read2st64_b32 v[2:3], v82 offset0:192 offset1:224
	s_waitcnt lgkmcnt(2)
	v_add_f32_e32 v6, v10, v6
	v_add_f32_e32 v6, v6, v7
	s_waitcnt lgkmcnt(1)
	v_add_f32_e32 v6, v6, v8
	v_add_f32_e32 v6, v6, v9
	s_waitcnt lgkmcnt(0)
	v_add_f32_e32 v2, v6, v2
	v_add_f32_e32 v2, v2, v3
	v_fma_f32 v2, -v4, v12, v2
	v_fmac_f32_e32 v5, v13, v2
	ds_write_b32 v83, v5
	s_waitcnt lgkmcnt(0)
	s_barrier
	s_and_saveexec_b64 s[36:37], s[82:83]
	s_cbranch_execz .LBB0_714
	ds_read_b32 v52, v84
	ds_read_b32 v34, v85
	ds_read_b32 v33, v86
	ds_read_b32 v32, v87
	ds_read_b32 v31, v88
	ds_read_b32 v30, v89
	ds_read_b32 v29, v90
	ds_read_b32 v28, v91
	ds_read_b32 v27, v92
	ds_read_b32 v26, v93
	ds_read_b32 v25, v94
	ds_read_b32 v24, v95
	ds_read_b32 v23, v96
	ds_read_b32 v22, v97
	ds_read_b32 v21, v98
	ds_read_b32 v20, v99
	ds_read_b32 v18, v100
	ds_read_b32 v17, v101
	ds_read_b32 v16, v102
	ds_read_b32 v15, v103
	ds_read_b32 v14, v104
	ds_read_b32 v13, v105
	ds_read_b32 v11, v106
	ds_read_b32 v10, v107
	ds_read_b32 v9, v108
	ds_read_b32 v8, v109
	ds_read_b32 v7, v110
	ds_read_b32 v6, v111
	ds_read_b32 v5, v112
	ds_read_b32 v4, v113
	ds_read_b32 v3, v114
	ds_read_b32 v2, v115
	s_waitcnt lgkmcnt(14)
	v_cmp_lg_f32_e32 vcc, s48, v52
	s_nop 1
	v_cndmask_b32_e32 v12, v143, v52, vcc
	v_cmp_gt_f32_e32 vcc, v34, v12
	s_nop 1
	v_cndmask_b32_e32 v12, v12, v34, vcc
	v_cndmask_b32_e64 v19, 0, 1, vcc
	v_cmp_gt_f32_e32 vcc, v33, v12
	s_nop 1
	v_cndmask_b32_e32 v12, v12, v33, vcc
	v_cndmask_b32_e64 v19, v19, 2, vcc
	v_cmp_gt_f32_e32 vcc, v32, v12
	s_nop 1
	v_cndmask_b32_e32 v12, v12, v32, vcc
	v_cndmask_b32_e64 v19, v19, 3, vcc
	v_cmp_gt_f32_e32 vcc, v31, v12
	s_nop 1
	v_cndmask_b32_e32 v12, v12, v31, vcc
	v_cndmask_b32_e64 v19, v19, 4, vcc
	v_cmp_gt_f32_e32 vcc, v30, v12
	s_nop 1
	v_cndmask_b32_e32 v12, v12, v30, vcc
	v_cndmask_b32_e64 v19, v19, 5, vcc
	v_cmp_gt_f32_e32 vcc, v29, v12
	s_nop 1
	v_cndmask_b32_e32 v12, v12, v29, vcc
	v_cndmask_b32_e64 v19, v19, 6, vcc
	v_cmp_gt_f32_e32 vcc, v28, v12
	s_nop 1
	v_cndmask_b32_e32 v12, v12, v28, vcc
	v_cndmask_b32_e64 v19, v19, 7, vcc
	v_cmp_gt_f32_e32 vcc, v27, v12
	s_nop 1
	v_cndmask_b32_e32 v12, v12, v27, vcc
	v_cndmask_b32_e64 v19, v19, 8, vcc
	v_cmp_gt_f32_e32 vcc, v26, v12
	s_nop 1
	v_cndmask_b32_e32 v12, v12, v26, vcc
	v_cndmask_b32_e64 v19, v19, 9, vcc
	v_cmp_gt_f32_e32 vcc, v25, v12
	s_nop 1
	v_cndmask_b32_e32 v12, v12, v25, vcc
	v_cndmask_b32_e64 v19, v19, 10, vcc
	v_cmp_gt_f32_e32 vcc, v24, v12
	s_nop 1
	v_cndmask_b32_e32 v12, v12, v24, vcc
	v_cndmask_b32_e64 v19, v19, 11, vcc
	v_cmp_gt_f32_e32 vcc, v23, v12
	s_nop 1
	v_cndmask_b32_e32 v12, v12, v23, vcc
	v_cndmask_b32_e64 v19, v19, 12, vcc
	v_cmp_gt_f32_e32 vcc, v22, v12
	s_nop 1
	v_cndmask_b32_e32 v12, v12, v22, vcc
	v_cndmask_b32_e64 v19, v19, 13, vcc
	v_cmp_gt_f32_e32 vcc, v21, v12
	s_nop 1
	v_cndmask_b32_e32 v12, v12, v21, vcc
	v_cndmask_b32_e64 v19, v19, 14, vcc
	v_cmp_gt_f32_e32 vcc, v20, v12
	s_nop 1
	v_cndmask_b32_e32 v12, v12, v20, vcc
	v_cndmask_b32_e64 v19, v19, 15, vcc
	v_cmp_gt_f32_e32 vcc, v18, v12
	s_nop 1
	v_cndmask_b32_e32 v12, v12, v18, vcc
	v_cndmask_b32_e64 v19, v19, 16, vcc
	v_cmp_gt_f32_e32 vcc, v17, v12
	s_nop 1
	v_cndmask_b32_e32 v12, v12, v17, vcc
	v_cndmask_b32_e64 v19, v19, 17, vcc
	s_waitcnt lgkmcnt(13)
	v_cmp_gt_f32_e32 vcc, v16, v12
	s_nop 1
	v_cndmask_b32_e32 v12, v12, v16, vcc
	v_cndmask_b32_e64 v19, v19, 18, vcc
	s_waitcnt lgkmcnt(12)
	v_cmp_gt_f32_e32 vcc, v15, v12
	s_nop 1
	v_cndmask_b32_e32 v12, v12, v15, vcc
	v_cndmask_b32_e64 v19, v19, 19, vcc
	s_waitcnt lgkmcnt(11)
	v_cmp_gt_f32_e32 vcc, v14, v12
	s_nop 1
	v_cndmask_b32_e32 v12, v12, v14, vcc
	v_cndmask_b32_e64 v19, v19, 20, vcc
	s_waitcnt lgkmcnt(10)
	v_cmp_gt_f32_e32 vcc, v13, v12
	s_nop 1
	v_cndmask_b32_e32 v12, v12, v13, vcc
	v_cndmask_b32_e64 v19, v19, 21, vcc
	s_waitcnt lgkmcnt(9)
	v_cmp_gt_f32_e32 vcc, v11, v12
	s_nop 1
	v_cndmask_b32_e32 v12, v12, v11, vcc
	v_cndmask_b32_e64 v19, v19, 22, vcc
	s_waitcnt lgkmcnt(8)
	v_cmp_gt_f32_e32 vcc, v10, v12
	s_nop 1
	v_cndmask_b32_e32 v12, v12, v10, vcc
	v_cndmask_b32_e64 v19, v19, 23, vcc
	s_waitcnt lgkmcnt(7)
	v_cmp_gt_f32_e32 vcc, v9, v12
	s_nop 1
	v_cndmask_b32_e32 v12, v12, v9, vcc
	v_cndmask_b32_e64 v19, v19, 24, vcc
	s_waitcnt lgkmcnt(6)
	v_cmp_gt_f32_e32 vcc, v8, v12
	s_nop 1
	v_cndmask_b32_e32 v12, v12, v8, vcc
	v_cndmask_b32_e64 v19, v19, 25, vcc
	s_waitcnt lgkmcnt(5)
	v_cmp_gt_f32_e32 vcc, v7, v12
	s_nop 1
	v_cndmask_b32_e32 v12, v12, v7, vcc
	v_cndmask_b32_e64 v19, v19, 26, vcc
	s_waitcnt lgkmcnt(4)
	v_cmp_gt_f32_e32 vcc, v6, v12
	s_nop 1
	v_cndmask_b32_e32 v12, v12, v6, vcc
	v_cndmask_b32_e64 v19, v19, 27, vcc
	s_waitcnt lgkmcnt(3)
	v_cmp_gt_f32_e32 vcc, v5, v12
	s_nop 1
	v_cndmask_b32_e32 v12, v12, v5, vcc
	v_cndmask_b32_e64 v19, v19, 28, vcc
	s_waitcnt lgkmcnt(2)
	v_cmp_gt_f32_e32 vcc, v4, v12
	s_nop 1
	v_cndmask_b32_e32 v12, v12, v4, vcc
	v_cndmask_b32_e64 v19, v19, 29, vcc
	s_waitcnt lgkmcnt(1)
	v_cmp_gt_f32_e32 vcc, v3, v12
	s_nop 1
	v_cndmask_b32_e32 v53, v12, v3, vcc
	v_cndmask_b32_e64 v19, v19, 30, vcc
	s_waitcnt lgkmcnt(0)
	v_cmp_gt_f32_e32 vcc, v2, v53
	s_nop 1
	v_cndmask_b32_e64 v12, v19, 31, vcc
	v_cndmask_b32_e32 v19, v53, v2, vcc
	v_cmp_eq_u32_e64 s[12:13], 0, v12
	v_cmp_nlg_f32_e32 vcc, s48, v52
	v_lshlrev_b32_e64 v53, v12, 1
	s_or_b64 s[12:13], s[12:13], vcc
	v_cndmask_b32_e64 v54, v52, v143, s[12:13]
	v_and_b32_e32 v55, 2, v53
	v_cmp_eq_u32_e64 s[12:13], 0, v55
	v_cmp_gt_f32_e64 s[14:15], v34, v54
	s_and_b64 s[12:13], s[12:13], s[14:15]
	v_cndmask_b32_e64 v54, v54, v34, s[12:13]
	v_and_b32_e32 v56, 4, v53
	v_cndmask_b32_e64 v55, 0, 1, s[12:13]
	v_cmp_eq_u32_e64 s[12:13], 0, v56
	v_cmp_gt_f32_e64 s[14:15], v33, v54
	s_and_b64 s[12:13], s[12:13], s[14:15]
	v_cndmask_b32_e64 v54, v54, v33, s[12:13]
	v_and_b32_e32 v56, 8, v53
	v_cndmask_b32_e64 v55, v55, 2, s[12:13]
	v_cmp_eq_u32_e64 s[12:13], 0, v56
	v_cmp_gt_f32_e64 s[14:15], v32, v54
	s_and_b64 s[12:13], s[12:13], s[14:15]
	v_cndmask_b32_e64 v54, v54, v32, s[12:13]
	v_and_b32_e32 v56, 16, v53
	v_cndmask_b32_e64 v55, v55, 3, s[12:13]
	v_cmp_eq_u32_e64 s[12:13], 0, v56
	v_cmp_gt_f32_e64 s[14:15], v31, v54
	s_and_b64 s[12:13], s[12:13], s[14:15]
	v_cndmask_b32_e64 v54, v54, v31, s[12:13]
	v_and_b32_e32 v56, 32, v53
	v_cndmask_b32_e64 v55, v55, 4, s[12:13]
	v_cmp_eq_u32_e64 s[12:13], 0, v56
	v_cmp_gt_f32_e64 s[14:15], v30, v54
	s_and_b64 s[12:13], s[12:13], s[14:15]
	v_cndmask_b32_e64 v54, v54, v30, s[12:13]
	v_and_b32_e32 v56, 64, v53
	v_cndmask_b32_e64 v55, v55, 5, s[12:13]
	v_cmp_eq_u32_e64 s[12:13], 0, v56
	v_cmp_gt_f32_e64 s[14:15], v29, v54
	s_and_b64 s[12:13], s[12:13], s[14:15]
	v_cndmask_b32_e64 v54, v54, v29, s[12:13]
	v_and_b32_e32 v56, 0x80, v53
	v_cndmask_b32_e64 v55, v55, 6, s[12:13]
	v_cmp_eq_u32_e64 s[12:13], 0, v56
	v_cmp_gt_f32_e64 s[14:15], v28, v54
	s_and_b64 s[12:13], s[12:13], s[14:15]
	v_cndmask_b32_e64 v54, v54, v28, s[12:13]
	v_and_b32_e32 v56, 0x100, v53
	v_cndmask_b32_e64 v55, v55, 7, s[12:13]
	v_cmp_eq_u32_e64 s[12:13], 0, v56
	v_cmp_gt_f32_e64 s[14:15], v27, v54
	s_and_b64 s[12:13], s[12:13], s[14:15]
	v_cndmask_b32_e64 v54, v54, v27, s[12:13]
	v_and_b32_e32 v56, 0x200, v53
	v_cndmask_b32_e64 v55, v55, 8, s[12:13]
	v_cmp_eq_u32_e64 s[12:13], 0, v56
	v_cmp_gt_f32_e64 s[14:15], v26, v54
	s_and_b64 s[12:13], s[12:13], s[14:15]
	v_cndmask_b32_e64 v54, v54, v26, s[12:13]
	v_and_b32_e32 v56, 0x400, v53
	v_cndmask_b32_e64 v55, v55, 9, s[12:13]
	v_cmp_eq_u32_e64 s[12:13], 0, v56
	v_cmp_gt_f32_e64 s[14:15], v25, v54
	s_and_b64 s[12:13], s[12:13], s[14:15]
	v_cndmask_b32_e64 v54, v54, v25, s[12:13]
	v_and_b32_e32 v56, 0x800, v53
	v_cndmask_b32_e64 v55, v55, 10, s[12:13]
	v_cmp_eq_u32_e64 s[12:13], 0, v56
	v_cmp_gt_f32_e64 s[14:15], v24, v54
	s_and_b64 s[12:13], s[12:13], s[14:15]
	v_cndmask_b32_e64 v54, v54, v24, s[12:13]
	v_and_b32_e32 v56, 0x1000, v53
	v_cndmask_b32_e64 v55, v55, 11, s[12:13]
	v_cmp_eq_u32_e64 s[12:13], 0, v56
	v_cmp_gt_f32_e64 s[14:15], v23, v54
	s_and_b64 s[12:13], s[12:13], s[14:15]
	v_cndmask_b32_e64 v54, v54, v23, s[12:13]
	v_and_b32_e32 v56, 0x2000, v53
	v_cndmask_b32_e64 v55, v55, 12, s[12:13]
	v_cmp_eq_u32_e64 s[12:13], 0, v56
	v_cmp_gt_f32_e64 s[14:15], v22, v54
	s_and_b64 s[12:13], s[12:13], s[14:15]
	v_cndmask_b32_e64 v54, v54, v22, s[12:13]
	v_and_b32_e32 v56, 0x4000, v53
	v_cndmask_b32_e64 v55, v55, 13, s[12:13]
	v_cmp_eq_u32_e64 s[12:13], 0, v56
	v_cmp_gt_f32_e64 s[14:15], v21, v54
	s_and_b64 s[12:13], s[12:13], s[14:15]
	v_cndmask_b32_e64 v54, v54, v21, s[12:13]
	v_and_b32_e32 v56, 0x8000, v53
	v_cndmask_b32_e64 v55, v55, 14, s[12:13]
	v_cmp_eq_u32_e64 s[12:13], 0, v56
	v_cmp_gt_f32_e64 s[14:15], v20, v54
	s_and_b64 s[12:13], s[12:13], s[14:15]
	v_cndmask_b32_e64 v54, v54, v20, s[12:13]
	v_and_b32_e32 v56, 0x10000, v53
	v_cndmask_b32_e64 v55, v55, 15, s[12:13]
	v_cmp_eq_u32_e64 s[12:13], 0, v56
	v_cmp_gt_f32_e64 s[14:15], v18, v54
	s_and_b64 s[12:13], s[12:13], s[14:15]
	v_cndmask_b32_e64 v54, v54, v18, s[12:13]
	v_and_b32_e32 v56, 0x20000, v53
	v_cndmask_b32_e64 v55, v55, 16, s[12:13]
	v_cmp_eq_u32_e64 s[12:13], 0, v56
	v_cmp_gt_f32_e64 s[14:15], v17, v54
	s_and_b64 s[12:13], s[12:13], s[14:15]
	v_cndmask_b32_e64 v54, v54, v17, s[12:13]
	v_and_b32_e32 v56, 0x40000, v53
	v_cndmask_b32_e64 v55, v55, 17, s[12:13]
	v_cmp_eq_u32_e64 s[12:13], 0, v56
	v_cmp_gt_f32_e64 s[14:15], v16, v54
	s_and_b64 s[12:13], s[12:13], s[14:15]
	v_cndmask_b32_e64 v54, v54, v16, s[12:13]
	v_and_b32_e32 v56, 0x80000, v53
	v_cndmask_b32_e64 v55, v55, 18, s[12:13]
	v_cmp_eq_u32_e64 s[12:13], 0, v56
	v_cmp_gt_f32_e64 s[14:15], v15, v54
	s_and_b64 s[12:13], s[12:13], s[14:15]
	v_cndmask_b32_e64 v54, v54, v15, s[12:13]
	v_and_b32_e32 v56, 0x100000, v53
	v_cndmask_b32_e64 v55, v55, 19, s[12:13]
	v_cmp_eq_u32_e64 s[12:13], 0, v56
	v_cmp_gt_f32_e64 s[14:15], v14, v54
	s_and_b64 s[12:13], s[12:13], s[14:15]
	v_cndmask_b32_e64 v54, v54, v14, s[12:13]
	v_and_b32_e32 v56, 0x200000, v53
	v_cndmask_b32_e64 v55, v55, 20, s[12:13]
	v_cmp_eq_u32_e64 s[12:13], 0, v56
	v_cmp_gt_f32_e64 s[14:15], v13, v54
	s_and_b64 s[12:13], s[12:13], s[14:15]
	v_cndmask_b32_e64 v54, v54, v13, s[12:13]
	v_and_b32_e32 v56, 0x400000, v53
	v_cndmask_b32_e64 v55, v55, 21, s[12:13]
	v_cmp_eq_u32_e64 s[12:13], 0, v56
	v_cmp_gt_f32_e64 s[14:15], v11, v54
	s_and_b64 s[12:13], s[12:13], s[14:15]
	v_cndmask_b32_e64 v54, v54, v11, s[12:13]
	v_and_b32_e32 v56, 0x800000, v53
	v_cndmask_b32_e64 v55, v55, 22, s[12:13]
	v_cmp_eq_u32_e64 s[12:13], 0, v56
	v_cmp_gt_f32_e64 s[14:15], v10, v54
	s_and_b64 s[12:13], s[12:13], s[14:15]
	v_cndmask_b32_e64 v54, v54, v10, s[12:13]
	v_and_b32_e32 v56, 0x1000000, v53
	v_cndmask_b32_e64 v55, v55, 23, s[12:13]
	v_cmp_eq_u32_e64 s[12:13], 0, v56
	v_cmp_gt_f32_e64 s[14:15], v9, v54
	s_and_b64 s[12:13], s[12:13], s[14:15]
	v_cndmask_b32_e64 v54, v54, v9, s[12:13]
	v_and_b32_e32 v56, 0x2000000, v53
	v_cndmask_b32_e64 v55, v55, 24, s[12:13]
	v_cmp_eq_u32_e64 s[12:13], 0, v56
	v_cmp_gt_f32_e64 s[14:15], v8, v54
	s_and_b64 s[12:13], s[12:13], s[14:15]
	v_cndmask_b32_e64 v54, v54, v8, s[12:13]
	v_and_b32_e32 v56, 0x4000000, v53
	v_cndmask_b32_e64 v55, v55, 25, s[12:13]
	v_cmp_eq_u32_e64 s[12:13], 0, v56
	v_cmp_gt_f32_e64 s[14:15], v7, v54
	s_and_b64 s[12:13], s[12:13], s[14:15]
	v_cndmask_b32_e64 v54, v54, v7, s[12:13]
	v_and_b32_e32 v56, 0x8000000, v53
	v_cndmask_b32_e64 v55, v55, 26, s[12:13]
	v_cmp_eq_u32_e64 s[12:13], 0, v56
	v_cmp_gt_f32_e64 s[14:15], v6, v54
	s_and_b64 s[12:13], s[12:13], s[14:15]
	v_cndmask_b32_e64 v54, v54, v6, s[12:13]
	v_and_b32_e32 v56, 0x10000000, v53
	v_cndmask_b32_e64 v55, v55, 27, s[12:13]
	v_cmp_eq_u32_e64 s[12:13], 0, v56
	v_cmp_gt_f32_e64 s[14:15], v5, v54
	s_and_b64 s[12:13], s[12:13], s[14:15]
	v_cndmask_b32_e64 v54, v54, v5, s[12:13]
	v_and_b32_e32 v56, 0x20000000, v53
	v_cndmask_b32_e64 v55, v55, 28, s[12:13]
	v_cmp_eq_u32_e64 s[12:13], 0, v56
	v_cmp_gt_f32_e64 s[14:15], v4, v54
	s_and_b64 s[12:13], s[12:13], s[14:15]
	v_cndmask_b32_e64 v54, v54, v4, s[12:13]
	v_and_b32_e32 v56, 2.0, v53
	v_cndmask_b32_e64 v55, v55, 29, s[12:13]
	v_cmp_eq_u32_e64 s[12:13], 0, v56
	v_cmp_gt_f32_e64 s[14:15], v3, v54
	s_and_b64 s[12:13], s[12:13], s[14:15]
	v_cndmask_b32_e64 v54, v54, v3, s[12:13]
	v_cndmask_b32_e64 v55, v55, 30, s[12:13]
	v_cmp_ne_u32_e64 s[12:13], 31, v12
	v_cmp_gt_f32_e64 s[14:15], v2, v54
	s_and_b64 s[12:13], s[12:13], s[14:15]
	v_cndmask_b32_e64 v55, v55, 31, s[12:13]
	v_lshl_or_b32 v53, 1, v55, v53
	v_and_b32_e32 v56, 1, v53
	v_cndmask_b32_e64 v54, v54, v2, s[12:13]
	v_cmp_eq_u32_e64 s[12:13], 1, v56
	s_or_b64 s[12:13], s[12:13], vcc
	v_and_b32_e32 v57, 2, v53
	v_cndmask_b32_e64 v56, v52, v143, s[12:13]
	v_cmp_eq_u32_e64 s[12:13], 0, v57
	v_cmp_gt_f32_e64 s[14:15], v34, v56
	s_and_b64 s[12:13], s[12:13], s[14:15]
	v_cndmask_b32_e64 v56, v56, v34, s[12:13]
	v_and_b32_e32 v58, 4, v53
	v_cndmask_b32_e64 v57, 0, 1, s[12:13]
	v_cmp_eq_u32_e64 s[12:13], 0, v58
	v_cmp_gt_f32_e64 s[14:15], v33, v56
	s_and_b64 s[12:13], s[12:13], s[14:15]
	v_cndmask_b32_e64 v56, v56, v33, s[12:13]
	v_and_b32_e32 v58, 8, v53
	v_cndmask_b32_e64 v57, v57, 2, s[12:13]
	v_cmp_eq_u32_e64 s[12:13], 0, v58
	v_cmp_gt_f32_e64 s[14:15], v32, v56
	s_and_b64 s[12:13], s[12:13], s[14:15]
	v_cndmask_b32_e64 v56, v56, v32, s[12:13]
	v_and_b32_e32 v58, 16, v53
	v_cndmask_b32_e64 v57, v57, 3, s[12:13]
	v_cmp_eq_u32_e64 s[12:13], 0, v58
	v_cmp_gt_f32_e64 s[14:15], v31, v56
	s_and_b64 s[12:13], s[12:13], s[14:15]
	v_cndmask_b32_e64 v56, v56, v31, s[12:13]
	v_and_b32_e32 v58, 32, v53
	v_cndmask_b32_e64 v57, v57, 4, s[12:13]
	v_cmp_eq_u32_e64 s[12:13], 0, v58
	v_cmp_gt_f32_e64 s[14:15], v30, v56
	s_and_b64 s[12:13], s[12:13], s[14:15]
	v_cndmask_b32_e64 v56, v56, v30, s[12:13]
	v_and_b32_e32 v58, 64, v53
	v_cndmask_b32_e64 v57, v57, 5, s[12:13]
	v_cmp_eq_u32_e64 s[12:13], 0, v58
	v_cmp_gt_f32_e64 s[14:15], v29, v56
	s_and_b64 s[12:13], s[12:13], s[14:15]
	v_cndmask_b32_e64 v56, v56, v29, s[12:13]
	v_and_b32_e32 v58, 0x80, v53
	v_cndmask_b32_e64 v57, v57, 6, s[12:13]
	v_cmp_eq_u32_e64 s[12:13], 0, v58
	v_cmp_gt_f32_e64 s[14:15], v28, v56
	s_and_b64 s[12:13], s[12:13], s[14:15]
	v_cndmask_b32_e64 v56, v56, v28, s[12:13]
	v_and_b32_e32 v58, 0x100, v53
	v_cndmask_b32_e64 v57, v57, 7, s[12:13]
	v_cmp_eq_u32_e64 s[12:13], 0, v58
	v_cmp_gt_f32_e64 s[14:15], v27, v56
	s_and_b64 s[12:13], s[12:13], s[14:15]
	v_cndmask_b32_e64 v56, v56, v27, s[12:13]
	v_and_b32_e32 v58, 0x200, v53
	v_cndmask_b32_e64 v57, v57, 8, s[12:13]
	v_cmp_eq_u32_e64 s[12:13], 0, v58
	v_cmp_gt_f32_e64 s[14:15], v26, v56
	s_and_b64 s[12:13], s[12:13], s[14:15]
	v_cndmask_b32_e64 v56, v56, v26, s[12:13]
	v_and_b32_e32 v58, 0x400, v53
	v_cndmask_b32_e64 v57, v57, 9, s[12:13]
	v_cmp_eq_u32_e64 s[12:13], 0, v58
	v_cmp_gt_f32_e64 s[14:15], v25, v56
	s_and_b64 s[12:13], s[12:13], s[14:15]
	v_cndmask_b32_e64 v56, v56, v25, s[12:13]
	v_and_b32_e32 v58, 0x800, v53
	v_cndmask_b32_e64 v57, v57, 10, s[12:13]
	v_cmp_eq_u32_e64 s[12:13], 0, v58
	v_cmp_gt_f32_e64 s[14:15], v24, v56
	s_and_b64 s[12:13], s[12:13], s[14:15]
	v_cndmask_b32_e64 v56, v56, v24, s[12:13]
	v_and_b32_e32 v58, 0x1000, v53
	v_cndmask_b32_e64 v57, v57, 11, s[12:13]
	v_cmp_eq_u32_e64 s[12:13], 0, v58
	v_cmp_gt_f32_e64 s[14:15], v23, v56
	s_and_b64 s[12:13], s[12:13], s[14:15]
	v_cndmask_b32_e64 v56, v56, v23, s[12:13]
	v_and_b32_e32 v58, 0x2000, v53
	v_cndmask_b32_e64 v57, v57, 12, s[12:13]
	v_cmp_eq_u32_e64 s[12:13], 0, v58
	v_cmp_gt_f32_e64 s[14:15], v22, v56
	s_and_b64 s[12:13], s[12:13], s[14:15]
	v_cndmask_b32_e64 v56, v56, v22, s[12:13]
	v_and_b32_e32 v58, 0x4000, v53
	v_cndmask_b32_e64 v57, v57, 13, s[12:13]
	v_cmp_eq_u32_e64 s[12:13], 0, v58
	v_cmp_gt_f32_e64 s[14:15], v21, v56
	s_and_b64 s[12:13], s[12:13], s[14:15]
	v_cndmask_b32_e64 v56, v56, v21, s[12:13]
	v_and_b32_e32 v58, 0x8000, v53
	v_cndmask_b32_e64 v57, v57, 14, s[12:13]
	v_cmp_eq_u32_e64 s[12:13], 0, v58
	v_cmp_gt_f32_e64 s[14:15], v20, v56
	s_and_b64 s[12:13], s[12:13], s[14:15]
	v_cndmask_b32_e64 v56, v56, v20, s[12:13]
	v_and_b32_e32 v58, 0x10000, v53
	v_cndmask_b32_e64 v57, v57, 15, s[12:13]
	v_cmp_eq_u32_e64 s[12:13], 0, v58
	v_cmp_gt_f32_e64 s[14:15], v18, v56
	s_and_b64 s[12:13], s[12:13], s[14:15]
	v_cndmask_b32_e64 v56, v56, v18, s[12:13]
	v_and_b32_e32 v58, 0x20000, v53
	v_cndmask_b32_e64 v57, v57, 16, s[12:13]
	v_cmp_eq_u32_e64 s[12:13], 0, v58
	v_cmp_gt_f32_e64 s[14:15], v17, v56
	s_and_b64 s[12:13], s[12:13], s[14:15]
	v_cndmask_b32_e64 v56, v56, v17, s[12:13]
	v_and_b32_e32 v58, 0x40000, v53
	v_cndmask_b32_e64 v57, v57, 17, s[12:13]
	v_cmp_eq_u32_e64 s[12:13], 0, v58
	v_cmp_gt_f32_e64 s[14:15], v16, v56
	s_and_b64 s[12:13], s[12:13], s[14:15]
	v_cndmask_b32_e64 v56, v56, v16, s[12:13]
	v_and_b32_e32 v58, 0x80000, v53
	v_cndmask_b32_e64 v57, v57, 18, s[12:13]
	v_cmp_eq_u32_e64 s[12:13], 0, v58
	v_cmp_gt_f32_e64 s[14:15], v15, v56
	s_and_b64 s[12:13], s[12:13], s[14:15]
	v_cndmask_b32_e64 v56, v56, v15, s[12:13]
	v_and_b32_e32 v58, 0x100000, v53
	v_cndmask_b32_e64 v57, v57, 19, s[12:13]
	v_cmp_eq_u32_e64 s[12:13], 0, v58
	v_cmp_gt_f32_e64 s[14:15], v14, v56
	s_and_b64 s[12:13], s[12:13], s[14:15]
	v_cndmask_b32_e64 v56, v56, v14, s[12:13]
	v_and_b32_e32 v58, 0x200000, v53
	v_cndmask_b32_e64 v57, v57, 20, s[12:13]
	v_cmp_eq_u32_e64 s[12:13], 0, v58
	v_cmp_gt_f32_e64 s[14:15], v13, v56
	s_and_b64 s[12:13], s[12:13], s[14:15]
	v_cndmask_b32_e64 v56, v56, v13, s[12:13]
	v_and_b32_e32 v58, 0x400000, v53
	v_cndmask_b32_e64 v57, v57, 21, s[12:13]
	v_cmp_eq_u32_e64 s[12:13], 0, v58
	v_cmp_gt_f32_e64 s[14:15], v11, v56
	s_and_b64 s[12:13], s[12:13], s[14:15]
	v_cndmask_b32_e64 v56, v56, v11, s[12:13]
	v_and_b32_e32 v58, 0x800000, v53
	v_cndmask_b32_e64 v57, v57, 22, s[12:13]
	v_cmp_eq_u32_e64 s[12:13], 0, v58
	v_cmp_gt_f32_e64 s[14:15], v10, v56
	s_and_b64 s[12:13], s[12:13], s[14:15]
	v_cndmask_b32_e64 v56, v56, v10, s[12:13]
	v_and_b32_e32 v58, 0x1000000, v53
	v_cndmask_b32_e64 v57, v57, 23, s[12:13]
	v_cmp_eq_u32_e64 s[12:13], 0, v58
	v_cmp_gt_f32_e64 s[14:15], v9, v56
	s_and_b64 s[12:13], s[12:13], s[14:15]
	v_cndmask_b32_e64 v56, v56, v9, s[12:13]
	v_and_b32_e32 v58, 0x2000000, v53
	v_cndmask_b32_e64 v57, v57, 24, s[12:13]
	v_cmp_eq_u32_e64 s[12:13], 0, v58
	v_cmp_gt_f32_e64 s[14:15], v8, v56
	s_and_b64 s[12:13], s[12:13], s[14:15]
	v_cndmask_b32_e64 v56, v56, v8, s[12:13]
	v_and_b32_e32 v58, 0x4000000, v53
	v_cndmask_b32_e64 v57, v57, 25, s[12:13]
	v_cmp_eq_u32_e64 s[12:13], 0, v58
	v_cmp_gt_f32_e64 s[14:15], v7, v56
	s_and_b64 s[12:13], s[12:13], s[14:15]
	v_cndmask_b32_e64 v56, v56, v7, s[12:13]
	v_and_b32_e32 v58, 0x8000000, v53
	v_cndmask_b32_e64 v57, v57, 26, s[12:13]
	v_cmp_eq_u32_e64 s[12:13], 0, v58
	v_cmp_gt_f32_e64 s[14:15], v6, v56
	s_and_b64 s[12:13], s[12:13], s[14:15]
	v_cndmask_b32_e64 v56, v56, v6, s[12:13]
	v_and_b32_e32 v58, 0x10000000, v53
	v_cndmask_b32_e64 v57, v57, 27, s[12:13]
	v_cmp_eq_u32_e64 s[12:13], 0, v58
	v_cmp_gt_f32_e64 s[14:15], v5, v56
	s_and_b64 s[12:13], s[12:13], s[14:15]
	v_cndmask_b32_e64 v56, v56, v5, s[12:13]
	v_and_b32_e32 v58, 0x20000000, v53
	v_cndmask_b32_e64 v57, v57, 28, s[12:13]
	v_cmp_eq_u32_e64 s[12:13], 0, v58
	v_cmp_gt_f32_e64 s[14:15], v4, v56
	s_and_b64 s[12:13], s[12:13], s[14:15]
	v_cndmask_b32_e64 v56, v56, v4, s[12:13]
	v_and_b32_e32 v58, 2.0, v53
	v_cndmask_b32_e64 v57, v57, 29, s[12:13]
	v_cmp_eq_u32_e64 s[12:13], 0, v58
	v_cmp_gt_f32_e64 s[14:15], v3, v56
	s_and_b64 s[12:13], s[12:13], s[14:15]
	v_cndmask_b32_e64 v56, v56, v3, s[12:13]
	v_cndmask_b32_e64 v57, v57, 30, s[12:13]
	v_cmp_lt_i32_e64 s[12:13], -1, v53
	v_cmp_gt_f32_e64 s[14:15], v2, v56
	s_and_b64 s[12:13], s[12:13], s[14:15]
	v_cndmask_b32_e64 v57, v57, 31, s[12:13]
	v_lshlrev_b32_e64 v58, v57, 1
	v_or_b32_e32 v59, v58, v53
	v_and_b32_e32 v60, 1, v59
	v_cndmask_b32_e64 v56, v56, v2, s[12:13]
	v_cmp_eq_u32_e64 s[12:13], 1, v60
	s_or_b64 vcc, s[12:13], vcc
	v_cndmask_b32_e32 v52, v52, v143, vcc
	v_bitop3_b32 v60, v58, 2, v53 bitop3:0xc8
	v_cmp_eq_u32_e32 vcc, 0, v60
	v_cmp_gt_f32_e64 s[12:13], v34, v52
	s_and_b64 vcc, vcc, s[12:13]
	v_cndmask_b32_e32 v34, v52, v34, vcc
	v_bitop3_b32 v52, v58, 4, v53 bitop3:0xc8
	v_cndmask_b32_e64 v60, 0, 1, vcc
	v_cmp_eq_u32_e32 vcc, 0, v52
	v_cmp_gt_f32_e64 s[12:13], v33, v34
	s_and_b64 vcc, vcc, s[12:13]
	v_cndmask_b32_e32 v33, v34, v33, vcc
	v_bitop3_b32 v34, v58, 8, v53 bitop3:0xc8
	v_cndmask_b32_e64 v52, v60, 2, vcc
	v_cmp_eq_u32_e32 vcc, 0, v34
	v_cmp_gt_f32_e64 s[12:13], v32, v33
	s_and_b64 vcc, vcc, s[12:13]
	v_cndmask_b32_e32 v32, v33, v32, vcc
	v_bitop3_b32 v33, v58, 16, v53 bitop3:0xc8
	v_cndmask_b32_e64 v34, v52, 3, vcc
	v_cmp_eq_u32_e32 vcc, 0, v33
	v_cmp_gt_f32_e64 s[12:13], v31, v32
	s_and_b64 vcc, vcc, s[12:13]
	v_cndmask_b32_e32 v31, v32, v31, vcc
	v_bitop3_b32 v32, v58, 32, v53 bitop3:0xc8
	v_cndmask_b32_e64 v33, v34, 4, vcc
	v_cmp_eq_u32_e32 vcc, 0, v32
	v_cmp_gt_f32_e64 s[12:13], v30, v31
	s_and_b64 vcc, vcc, s[12:13]
	v_cndmask_b32_e32 v30, v31, v30, vcc
	v_bitop3_b32 v31, v58, 64, v53 bitop3:0xc8
	v_cndmask_b32_e64 v32, v33, 5, vcc
	v_cmp_eq_u32_e32 vcc, 0, v31
	v_cmp_gt_f32_e64 s[12:13], v29, v30
	s_and_b64 vcc, vcc, s[12:13]
	v_cndmask_b32_e32 v29, v30, v29, vcc
	v_bitop3_b32 v30, v58, s49, v53 bitop3:0xc8
	v_cndmask_b32_e64 v31, v32, 6, vcc
	v_cmp_eq_u32_e32 vcc, 0, v30
	v_cmp_gt_f32_e64 s[12:13], v28, v29
	s_and_b64 vcc, vcc, s[12:13]
	v_cndmask_b32_e32 v28, v29, v28, vcc
	v_bitop3_b32 v29, v58, s39, v53 bitop3:0xc8
	v_cndmask_b32_e64 v30, v31, 7, vcc
	v_cmp_eq_u32_e32 vcc, 0, v29
	v_cmp_gt_f32_e64 s[12:13], v27, v28
	s_and_b64 vcc, vcc, s[12:13]
	s_movk_i32 s12, 0x200
	v_cndmask_b32_e32 v27, v28, v27, vcc
	v_bitop3_b32 v28, v58, s12, v53 bitop3:0xc8
	v_cndmask_b32_e64 v29, v30, 8, vcc
	v_cmp_eq_u32_e32 vcc, 0, v28
	v_cmp_gt_f32_e64 s[12:13], v26, v27
	s_and_b64 vcc, vcc, s[12:13]
	s_movk_i32 s12, 0x400
	v_cndmask_b32_e32 v26, v27, v26, vcc
	v_bitop3_b32 v27, v58, s12, v53 bitop3:0xc8
	v_cndmask_b32_e64 v28, v29, 9, vcc
	v_cmp_eq_u32_e32 vcc, 0, v27
	v_cmp_gt_f32_e64 s[12:13], v25, v26
	s_and_b64 vcc, vcc, s[12:13]
	v_cndmask_b32_e32 v25, v26, v25, vcc
	v_bitop3_b32 v26, v58, s3, v53 bitop3:0xc8
	v_cndmask_b32_e64 v27, v28, 10, vcc
	v_cmp_eq_u32_e32 vcc, 0, v26
	v_cmp_gt_f32_e64 s[12:13], v24, v25
	s_and_b64 vcc, vcc, s[12:13]
	v_cndmask_b32_e32 v24, v25, v24, vcc
	v_bitop3_b32 v25, v58, s50, v53 bitop3:0xc8
	v_cndmask_b32_e64 v26, v27, 11, vcc
	v_cmp_eq_u32_e32 vcc, 0, v25
	v_cmp_gt_f32_e64 s[12:13], v23, v24
	s_and_b64 vcc, vcc, s[12:13]
	v_cndmask_b32_e32 v23, v24, v23, vcc
	v_bitop3_b32 v24, v58, s51, v53 bitop3:0xc8
	v_cndmask_b32_e64 v25, v26, 12, vcc
	v_cmp_eq_u32_e32 vcc, 0, v24
	v_cmp_gt_f32_e64 s[12:13], v22, v23
	s_and_b64 vcc, vcc, s[12:13]
	v_cndmask_b32_e32 v22, v23, v22, vcc
	v_bitop3_b32 v23, v58, s52, v53 bitop3:0xc8
	v_cndmask_b32_e64 v24, v25, 13, vcc
	v_cmp_eq_u32_e32 vcc, 0, v23
	v_cmp_gt_f32_e64 s[12:13], v21, v22
	s_and_b64 vcc, vcc, s[12:13]
	v_cndmask_b32_e32 v21, v22, v21, vcc
	v_bitop3_b32 v22, v58, s53, v53 bitop3:0xc8
	v_cndmask_b32_e64 v23, v24, 14, vcc
	v_cmp_eq_u32_e32 vcc, 0, v22
	v_cmp_gt_f32_e64 s[12:13], v20, v21
	s_and_b64 vcc, vcc, s[12:13]
	s_mov_b32 s12, 0x10000
	v_cndmask_b32_e32 v20, v21, v20, vcc
	v_bitop3_b32 v21, v58, s12, v53 bitop3:0xc8
	v_cndmask_b32_e64 v22, v23, 15, vcc
	v_cmp_eq_u32_e32 vcc, 0, v21
	v_cmp_gt_f32_e64 s[12:13], v18, v20
	s_and_b64 vcc, vcc, s[12:13]
	v_cndmask_b32_e32 v18, v20, v18, vcc
	v_bitop3_b32 v20, v58, s54, v53 bitop3:0xc8
	v_cndmask_b32_e64 v21, v22, 16, vcc
	v_cmp_eq_u32_e32 vcc, 0, v20
	v_cmp_gt_f32_e64 s[12:13], v17, v18
	s_and_b64 vcc, vcc, s[12:13]
	v_cndmask_b32_e32 v17, v18, v17, vcc
	v_bitop3_b32 v18, v58, s55, v53 bitop3:0xc8
	v_cndmask_b32_e64 v20, v21, 17, vcc
	v_cmp_eq_u32_e32 vcc, 0, v18
	v_cmp_gt_f32_e64 s[12:13], v16, v17
	s_and_b64 vcc, vcc, s[12:13]
	v_cndmask_b32_e32 v16, v17, v16, vcc
	v_bitop3_b32 v17, v58, s56, v53 bitop3:0xc8
	v_cndmask_b32_e64 v18, v20, 18, vcc
	v_cmp_eq_u32_e32 vcc, 0, v17
	v_cmp_gt_f32_e64 s[12:13], v15, v16
	s_and_b64 vcc, vcc, s[12:13]
	v_cndmask_b32_e32 v15, v16, v15, vcc
	v_bitop3_b32 v16, v58, s57, v53 bitop3:0xc8
	v_cndmask_b32_e64 v17, v18, 19, vcc
	v_cmp_eq_u32_e32 vcc, 0, v16
	v_cmp_gt_f32_e64 s[12:13], v14, v15
	s_and_b64 vcc, vcc, s[12:13]
	v_cndmask_b32_e32 v14, v15, v14, vcc
	v_bitop3_b32 v15, v58, s58, v53 bitop3:0xc8
	v_cndmask_b32_e64 v16, v17, 20, vcc
	v_cmp_eq_u32_e32 vcc, 0, v15
	v_cmp_gt_f32_e64 s[12:13], v13, v14
	s_and_b64 vcc, vcc, s[12:13]
	v_cndmask_b32_e32 v13, v14, v13, vcc
	v_bitop3_b32 v14, v58, s59, v53 bitop3:0xc8
	v_cndmask_b32_e64 v15, v16, 21, vcc
	v_cmp_eq_u32_e32 vcc, 0, v14
	v_cmp_gt_f32_e64 s[12:13], v11, v13
	s_and_b64 vcc, vcc, s[12:13]
	v_cndmask_b32_e32 v11, v13, v11, vcc
	v_bitop3_b32 v13, v58, s60, v53 bitop3:0xc8
	v_cndmask_b32_e64 v14, v15, 22, vcc
	v_cmp_eq_u32_e32 vcc, 0, v13
	v_cmp_gt_f32_e64 s[12:13], v10, v11
	s_and_b64 vcc, vcc, s[12:13]
	v_cndmask_b32_e32 v10, v11, v10, vcc
	v_bitop3_b32 v11, v58, s61, v53 bitop3:0xc8
	v_cndmask_b32_e64 v13, v14, 23, vcc
	v_cmp_eq_u32_e32 vcc, 0, v11
	v_cmp_gt_f32_e64 s[12:13], v9, v10
	s_and_b64 vcc, vcc, s[12:13]
	v_cndmask_b32_e32 v9, v10, v9, vcc
	v_bitop3_b32 v10, v58, s62, v53 bitop3:0xc8
	v_cndmask_b32_e64 v11, v13, 24, vcc
	v_cmp_eq_u32_e32 vcc, 0, v10
	v_cmp_gt_f32_e64 s[12:13], v8, v9
	s_and_b64 vcc, vcc, s[12:13]
	v_cndmask_b32_e32 v8, v9, v8, vcc
	v_bitop3_b32 v9, v58, s63, v53 bitop3:0xc8
	v_cndmask_b32_e64 v10, v11, 25, vcc
	v_cmp_eq_u32_e32 vcc, 0, v9
	v_cmp_gt_f32_e64 s[12:13], v7, v8
	s_and_b64 vcc, vcc, s[12:13]
	v_cndmask_b32_e32 v7, v8, v7, vcc
	v_bitop3_b32 v8, v58, s64, v53 bitop3:0xc8
	v_cndmask_b32_e64 v9, v10, 26, vcc
	v_cmp_eq_u32_e32 vcc, 0, v8
	v_cmp_gt_f32_e64 s[12:13], v6, v7
	s_and_b64 vcc, vcc, s[12:13]
	v_cndmask_b32_e32 v6, v7, v6, vcc
	v_bitop3_b32 v7, v58, s65, v53 bitop3:0xc8
	v_cndmask_b32_e64 v8, v9, 27, vcc
	v_cmp_eq_u32_e32 vcc, 0, v7
	v_cmp_gt_f32_e64 s[12:13], v5, v6
	s_and_b64 vcc, vcc, s[12:13]
	v_cndmask_b32_e32 v5, v6, v5, vcc
	v_bitop3_b32 v6, v58, s66, v53 bitop3:0xc8
	v_cndmask_b32_e64 v7, v8, 28, vcc
	v_cmp_eq_u32_e32 vcc, 0, v6
	v_cmp_gt_f32_e64 s[12:13], v4, v5
	s_and_b64 vcc, vcc, s[12:13]
	v_cndmask_b32_e32 v4, v5, v4, vcc
	v_bitop3_b32 v5, v58, 2.0, v53 bitop3:0xc8
	v_cndmask_b32_e64 v6, v7, 29, vcc
	v_cmp_eq_u32_e32 vcc, 0, v5
	v_cmp_gt_f32_e64 s[12:13], v3, v4
	s_and_b64 vcc, vcc, s[12:13]
	v_cndmask_b32_e32 v3, v4, v3, vcc
	v_cndmask_b32_e64 v5, v6, 30, vcc
	v_cmp_lt_i32_e32 vcc, -1, v59
	v_cmp_gt_f32_e64 s[12:13], v2, v3
	s_and_b64 vcc, vcc, s[12:13]
	v_cndmask_b32_e32 v2, v3, v2, vcc
	v_sub_f32_e32 v3, v54, v19
	v_cndmask_b32_e64 v4, v5, 31, vcc
	v_mul_f32_e32 v3, 0x3fb8aa3b, v3
	v_sub_f32_e32 v5, v56, v19
	v_exp_f32_e32 v3, v3
	v_mul_f32_e32 v5, 0x3fb8aa3b, v5
	v_sub_f32_e32 v2, v2, v19
	v_exp_f32_e32 v5, v5
	v_mul_f32_e32 v2, 0x3fb8aa3b, v2
	v_exp_f32_e32 v2, v2
	v_add_f32_e32 v6, 1.0, v3
	v_add_f32_e32 v6, v6, v5
	v_add_f32_e32 v6, v6, v2
	v_div_scale_f32 v7, s[12:13], v6, v6, 1.0
	v_rcp_f32_e32 v8, v7
	s_nop 0
	v_fma_f32 v9, -v7, v8, 1.0
	v_fmac_f32_e32 v8, v9, v8
	v_div_scale_f32 v9, vcc, 1.0, v6, 1.0
	v_mul_f32_e32 v10, v9, v8
	v_fma_f32 v11, -v7, v10, v9
	v_fmac_f32_e32 v10, v11, v8
	v_fma_f32 v7, -v7, v10, v9
	v_div_fmas_f32 v7, v7, v8, v10
	v_div_fixup_f32 v6, v7, v6, 1.0
	ds_write_b32 v116, v12
	ds_write_b32 v117, v6
	v_lshl_add_u32 v7, v12, 2, s38
	ds_add_rtn_u32 v7, v7, v142
	v_mul_f32_e32 v3, v3, v6
	s_waitcnt lgkmcnt(0)
	ds_write_b32 v118, v7
	ds_write_b32 v119, v55
	ds_write_b32 v120, v3
	v_lshl_add_u32 v3, v55, 2, s38
	ds_add_rtn_u32 v3, v3, v142
	v_mul_f32_e32 v5, v5, v6
	s_waitcnt lgkmcnt(0)
	ds_write_b32 v121, v3
	ds_write_b32 v122, v57
	ds_write_b32 v123, v5
	v_lshl_add_u32 v3, v57, 2, s38
	ds_add_rtn_u32 v3, v3, v142
	v_mul_f32_e32 v2, v2, v6
	s_waitcnt lgkmcnt(0)
	ds_write_b32 v124, v3
	ds_write_b32 v125, v4
	ds_write_b32 v126, v2
	v_lshl_add_u32 v2, v4, 2, s38
	ds_add_rtn_u32 v2, v2, v142
	s_waitcnt lgkmcnt(0)
	ds_write_b32 v127, v2
